# linmap
# speedup vs baseline: 1.0611x; 1.0611x over previous
_Z10gae_kernelPKfPKiS2_S0_S0_S0_PfS3_:
	s_load_dwordx8 s[4:11], s[0:1], 0x0
	s_load_dwordx4 s[12:15], s[0:1], 0x20
	v_and_b32_e32 v64, 63, v0
	v_lshrrev_b32_e32 v1, 6, v0
	s_mov_b32 s3, 0
	s_lshl_b64 s[2:3], s[2:3], 11
	v_lshlrev_b32_e32 v2, 9, v1
	v_lshlrev_b32_e32 v3, 2, v64
	v_or3_b32 v2, s2, v2, v3
	v_mov_b32_e32 v3, s3
	v_lshlrev_b64 v[18:19], 2, v[2:3]
	s_waitcnt lgkmcnt(0)
	v_lshl_add_u64 v[54:55], s[14:15], 0, v[18:19]
	v_lshl_add_u64 v[52:53], s[6:7], 0, v[18:19]
	global_load_dwordx4 v[10:13], v[54:55], off nt
	global_load_dwordx4 v[14:17], v[52:53], off nt
	v_lshl_add_u64 v[56:57], s[8:9], 0, v[18:19]
	global_load_dwordx4 v[20:23], v[56:57], off nt
	v_lshl_add_u64 v[58:59], s[12:13], 0, v[18:19]
	global_load_dwordx4 v[24:27], v[58:59], off nt
	v_lshl_add_u64 v[60:61], s[4:5], 0, v[18:19]
	global_load_dwordx4 v[28:31], v[60:61], off nt
	v_lshl_add_u64 v[62:63], s[10:11], 0, v[18:19]
	global_load_dwordx4 v[2:5], v[62:63], off nt
	global_load_dwordx4 v[32:35], v[60:61], off offset:1024 nt
	global_load_dwordx4 v[36:39], v[52:53], off offset:1024 nt
	global_load_dwordx4 v[40:43], v[56:57], off offset:1024 nt
	global_load_dwordx4 v[6:9], v[62:63], off offset:1024 nt
	global_load_dwordx4 v[44:47], v[58:59], off offset:1024 nt
	global_load_dwordx4 v[48:51], v[54:55], off offset:1024 nt
	v_mov_b32_e32 v66, 0
	v_mov_b32_e32 v68, 1.0
	v_mov_b32_e32 v69, 0
	v_mov_b32_e32 v70, 1.0
	v_mov_b32_e32 v71, 0
	v_mov_b32_e32 v72, 1.0
	v_bfe_u32 v73, v0, 4, 2
	v_cmp_gt_u32_e64 s[4:5], 16, v64
	v_mov_b32_e32 v65, 0
	v_mov_b32_e32 v67, 1.0
	s_waitcnt vmcnt(11)
	v_mul_f32_e32 v12, 0x3f7d70a4, v12
	s_waitcnt vmcnt(10)
	v_cmp_eq_u32_e32 vcc, 0, v14
	v_mul_f32_e32 v13, 0x3f7d70a4, v13
	v_mul_f32_e32 v10, 0x3f7d70a4, v10
	v_cndmask_b32_e64 v14, 0, 1.0, vcc
	s_waitcnt vmcnt(9)
	v_cmp_eq_u32_e32 vcc, 0, v20
	v_mul_f32_e32 v11, 0x3f7d70a4, v11
	s_waitcnt vmcnt(8)
	v_mul_f32_e32 v26, v26, v12
	v_cndmask_b32_e64 v20, 0, 1.0, vcc
	v_cmp_eq_u32_e32 vcc, 0, v15
	v_mul_f32_e32 v27, v27, v13
	v_mul_f32_e32 v24, v24, v10
	v_cndmask_b32_e64 v15, 0, 1.0, vcc
	v_cmp_eq_u32_e32 vcc, 0, v21
	v_mul_f32_e32 v25, v25, v11
	v_mul_f32_e32 v12, 0x3f733333, v12
	v_cndmask_b32_e64 v21, 0, 1.0, vcc
	v_cmp_eq_u32_e32 vcc, 0, v16
	v_mul_f32_e32 v13, 0x3f733333, v13
	v_mul_f32_e32 v10, 0x3f733333, v10
	v_cndmask_b32_e64 v16, 0, 1.0, vcc
	v_cmp_eq_u32_e32 vcc, 0, v22
	s_waitcnt vmcnt(7)
	v_fma_f32 v16, v26, v16, v30
	v_mul_f32_e32 v11, 0x3f733333, v11
	v_cndmask_b32_e64 v22, 0, 1.0, vcc
	v_cmp_eq_u32_e32 vcc, 0, v17
	v_fma_f32 v14, v24, v14, v28
	v_fma_f32 v15, v25, v15, v29
	v_cndmask_b32_e64 v17, 0, 1.0, vcc
	v_cmp_eq_u32_e32 vcc, 0, v23
	v_fmac_f32_e32 v31, v27, v17
	v_mul_f32_e32 v22, v12, v22
	v_cndmask_b32_e64 v23, 0, 1.0, vcc
	v_mul_f32_e32 v23, v13, v23
	s_waitcnt vmcnt(6)
	v_sub_f32_e32 v12, v16, v4
	v_sub_f32_e32 v13, v31, v5
	v_mul_f32_e32 v20, v10, v20
	v_mul_f32_e32 v21, v11, v21
	v_sub_f32_e32 v10, v14, v2
	v_sub_f32_e32 v11, v15, v3
	v_mul_f32_e32 v14, v23, v22
	v_fma_f32 v15, v22, v13, v12
	v_mul_f32_e32 v14, v14, v21
	v_fma_f32 v15, v21, v15, v11
	v_mul_f32_e32 v14, v14, v20
	v_fma_f32 v24, v20, v15, v10
	v_mov_b32_e32 v16, 1.0
	v_mov_b32_dpp v68, v14 row_shl:1 row_mask:0xf bank_mask:0xf
	v_mov_b32_dpp v66, v24 row_shl:1 row_mask:0xf bank_mask:0xf
	v_mul_f32_e32 v15, v14, v68
	v_fmac_f32_e32 v24, v14, v66
	v_cmp_eq_u32_e32 vcc, 2, v73
	v_mov_b32_dpp v70, v15 row_shl:2 row_mask:0xf bank_mask:0xf
	v_mov_b32_dpp v69, v24 row_shl:2 row_mask:0xf bank_mask:0xf
	v_mul_f32_e32 v14, v15, v70
	v_fmac_f32_e32 v24, v15, v69
	v_mov_b32_e32 v15, 0
	v_mov_b32_dpp v72, v14 row_shl:4 row_mask:0xf bank_mask:0xf
	v_mov_b32_dpp v71, v24 row_shl:4 row_mask:0xf bank_mask:0xf
	v_fmac_f32_e32 v24, v14, v71
	v_mul_f32_e32 v14, v14, v72
	s_nop 0
	v_mov_b32_dpp v15, v24 row_shl:8 row_mask:0xf bank_mask:0xf
	v_mov_b32_dpp v16, v14 row_shl:8 row_mask:0xf bank_mask:0xf
	v_fmac_f32_e32 v24, v14, v15
	v_mul_f32_e32 v14, v14, v16
	v_readlane_b32 s9, v24, 32
	v_readlane_b32 s2, v14, 48
	v_readlane_b32 s8, v14, 32
	v_readlane_b32 s6, v14, 16
	v_mov_b32_e32 v15, s2
	v_mul_f32_e32 v16, s8, v15
	v_cndmask_b32_e32 v15, 1.0, v15, vcc
	v_cmp_eq_u32_e64 s[2:3], 1, v73
	v_readlane_b32 s10, v24, 48
	v_mul_f32_e32 v17, s6, v16
	v_cndmask_b32_e64 v15, v15, v16, s[2:3]
	v_readlane_b32 s7, v24, 16
	v_cndmask_b32_e64 v15, v15, v17, s[4:5]
	v_mov_b32_e32 v16, s9
	v_mov_b32_e32 v17, s10
	v_fmac_f32_e32 v16, s8, v17
	v_mov_b32_e32 v25, s7
	v_cndmask_b32_e32 v17, 0, v17, vcc
	v_fmac_f32_e32 v25, s6, v16
	v_cndmask_b32_e64 v16, v17, v16, s[2:3]
	v_cndmask_b32_e64 v16, v16, v25, s[4:5]
	s_waitcnt vmcnt(4)
	v_cmp_eq_u32_e64 s[6:7], 0, v36
	v_fmac_f32_e32 v24, v14, v16
	v_mul_f32_e32 v28, v14, v15
	s_waitcnt vmcnt(0)
	v_mul_f32_e32 v15, 0x3f7d70a4, v48
	v_cndmask_b32_e64 v14, 0, 1.0, s[6:7]
	v_cmp_eq_u32_e64 s[6:7], 0, v40
	v_mul_f32_e32 v17, v44, v15
	v_mul_f32_e32 v15, 0x3f733333, v15
	v_cndmask_b32_e64 v16, 0, 1.0, s[6:7]
	v_cmp_eq_u32_e64 s[6:7], 0, v37
	v_mul_f32_e32 v25, v15, v16
	v_mul_f32_e32 v16, 0x3f7d70a4, v49
	v_cndmask_b32_e64 v15, 0, 1.0, s[6:7]
	v_cmp_eq_u32_e64 s[6:7], 0, v41
	v_fma_f32 v14, v17, v14, v32
	v_mul_f32_e32 v26, v45, v16
	v_cndmask_b32_e64 v17, 0, 1.0, s[6:7]
	v_mul_f32_e32 v16, 0x3f733333, v16
	v_fma_f32 v15, v26, v15, v33
	v_mul_f32_e32 v26, v16, v17
	v_mul_f32_e32 v17, 0x3f7d70a4, v50
	v_cmp_eq_u32_e64 s[6:7], 0, v38
	v_mul_f32_e32 v29, v46, v17
	v_mul_f32_e32 v17, 0x3f733333, v17
	v_cndmask_b32_e64 v16, 0, 1.0, s[6:7]
	v_cmp_eq_u32_e64 s[6:7], 0, v42
	v_fma_f32 v16, v29, v16, v34
	v_mul_f32_e32 v29, 0x3f7d70a4, v51
	v_cndmask_b32_e64 v27, 0, 1.0, s[6:7]
	v_cmp_eq_u32_e64 s[6:7], 0, v39
	v_mul_f32_e32 v27, v17, v27
	v_mul_f32_e32 v31, v47, v29
	v_cndmask_b32_e64 v17, 0, 1.0, s[6:7]
	v_cmp_eq_u32_e64 s[6:7], 0, v43
	v_fmac_f32_e32 v35, v31, v17
	v_mul_f32_e32 v29, 0x3f733333, v29
	v_cndmask_b32_e64 v30, 0, 1.0, s[6:7]
	v_sub_f32_e32 v16, v16, v8
	v_sub_f32_e32 v17, v35, v9
	v_mul_f32_e32 v29, v29, v30
	v_sub_f32_e32 v15, v15, v7
	v_fma_f32 v30, v27, v17, v16
	v_mul_f32_e32 v31, v29, v27
	v_sub_f32_e32 v14, v14, v6
	v_fma_f32 v30, v26, v30, v15
	v_mul_f32_e32 v31, v31, v26
	v_fma_f32 v30, v25, v30, v14
	v_mul_f32_e32 v31, v31, v25
	v_mov_b32_e32 v32, 0
	v_mov_b32_e32 v33, 1.0
	s_nop 0
	v_mov_b32_dpp v32, v30 row_shl:1 row_mask:0xf bank_mask:0xf
	v_mov_b32_dpp v33, v31 row_shl:1 row_mask:0xf bank_mask:0xf
	v_fmac_f32_e32 v30, v31, v32
	v_mul_f32_e32 v31, v31, v33
	v_mov_b32_e32 v32, 0
	v_mov_b32_e32 v33, 1.0
	s_nop 0
	v_mov_b32_dpp v32, v30 row_shl:2 row_mask:0xf bank_mask:0xf
	v_mov_b32_dpp v33, v31 row_shl:2 row_mask:0xf bank_mask:0xf
	v_fmac_f32_e32 v30, v31, v32
	v_mul_f32_e32 v31, v31, v33
	v_mov_b32_e32 v32, 0
	v_mov_b32_e32 v33, 1.0
	s_nop 0
	v_mov_b32_dpp v32, v30 row_shl:4 row_mask:0xf bank_mask:0xf
	v_mov_b32_dpp v33, v31 row_shl:4 row_mask:0xf bank_mask:0xf
	v_fmac_f32_e32 v30, v31, v32
	v_mul_f32_e32 v31, v31, v33
	s_nop 0
	v_mov_b32_dpp v65, v30 row_shl:8 row_mask:0xf bank_mask:0xf
	v_mov_b32_dpp v67, v31 row_shl:8 row_mask:0xf bank_mask:0xf
	v_fmac_f32_e32 v30, v31, v65
	v_mul_f32_e32 v31, v31, v67
	v_readlane_b32 s9, v30, 32
	v_readlane_b32 s10, v31, 48
	v_readlane_b32 s8, v31, 32
	v_readlane_b32 s6, v31, 16
	v_mov_b32_e32 v32, s10
	v_mul_f32_e32 v33, s8, v32
	v_cndmask_b32_e32 v32, 1.0, v32, vcc
	v_readlane_b32 s11, v30, 48
	v_mul_f32_e32 v34, s6, v33
	v_cndmask_b32_e64 v32, v32, v33, s[2:3]
	v_readlane_b32 s7, v30, 16
	v_cndmask_b32_e64 v32, v32, v34, s[4:5]
	v_mov_b32_e32 v33, s9
	v_mov_b32_e32 v34, s11
	v_fmac_f32_e32 v33, s8, v34
	v_mov_b32_e32 v35, s7
	v_cndmask_b32_e32 v34, 0, v34, vcc
	v_fmac_f32_e32 v35, s6, v33
	v_cndmask_b32_e64 v33, v34, v33, s[2:3]
	v_cndmask_b32_e64 v33, v33, v35, s[4:5]
	v_fmac_f32_e32 v30, v31, v33
	v_mul_f32_e32 v31, v31, v32
	v_readlane_b32 s6, v28, 0
	v_readlane_b32 s7, v24, 0
	v_readlane_b32 s4, v31, 0
	v_readlane_b32 s5, v30, 0
	v_cmp_eq_u32_e32 vcc, 0, v64
	s_and_saveexec_b64 s[2:3], vcc
	s_cbranch_execz .LBB0_4
	v_mov_b32_e32 v32, s4
	v_mov_b32_e32 v33, s7
	v_mov_b32_e32 v34, s5
	v_mul_f32_e32 v32, s6, v32
	v_lshlrev_b32_e32 v1, 2, v1
	v_fmac_f32_e32 v33, s6, v34
	ds_write2_b32 v1, v32, v33 offset1:4

	.amdhsa_kernel _Z10gae_kernelPKfPKiS2_S0_S0_S0_PfS3_
		.amdhsa_group_segment_fixed_size 81664
		.amdhsa_private_segment_fixed_size 0
		.amdhsa_kernarg_size 64
		.amdhsa_user_sgpr_count 2
		.amdhsa_user_sgpr_dispatch_ptr 0
		.amdhsa_user_sgpr_queue_ptr 0
		.amdhsa_user_sgpr_kernarg_segment_ptr 1
		.amdhsa_user_sgpr_dispatch_id 0
		.amdhsa_user_sgpr_kernarg_preload_length 0
		.amdhsa_user_sgpr_kernarg_preload_offset 0
		.amdhsa_user_sgpr_private_segment_size 0
		.amdhsa_uses_dynamic_stack 0
		.amdhsa_enable_private_segment 0
		.amdhsa_system_sgpr_workgroup_id_x 1
		.amdhsa_system_sgpr_workgroup_id_y 0
		.amdhsa_system_sgpr_workgroup_id_z 0
		.amdhsa_system_sgpr_workgroup_info 0
		.amdhsa_system_vgpr_workitem_id 0
		.amdhsa_next_free_vgpr 80
		.amdhsa_next_free_sgpr 96
		.amdhsa_accum_offset 76
		.amdhsa_reserve_vcc 1
		.amdhsa_float_round_mode_32 0
		.amdhsa_float_round_mode_16_64 0
		.amdhsa_float_denorm_mode_32 3
		.amdhsa_float_denorm_mode_16_64 3
		.amdhsa_dx10_clamp 1
		.amdhsa_ieee_mode 1
		.amdhsa_fp16_overflow 0
		.amdhsa_tg_split 0
		.amdhsa_exception_fp_ieee_invalid_op 0
		.amdhsa_exception_fp_denorm_src 0
		.amdhsa_exception_fp_ieee_div_zero 0
		.amdhsa_exception_fp_ieee_overflow 0
		.amdhsa_exception_fp_ieee_underflow 0
		.amdhsa_exception_fp_ieee_inexact 0
		.amdhsa_exception_int_div_zero 0
	.end_amdhsa_kernel

amdhsa.kernels:
  - .agpr_count:     0
    .args:
      - .actual_access:  read_only
        .address_space:  global
        .offset:         0
        .size:           8
        .value_kind:     global_buffer
      - .actual_access:  read_only
        .address_space:  global
        .offset:         8
        .size:           8
        .value_kind:     global_buffer
      - .actual_access:  read_only
        .address_space:  global
        .offset:         16
        .size:           8
        .value_kind:     global_buffer
      - .actual_access:  read_only
        .address_space:  global
        .offset:         24
        .size:           8
        .value_kind:     global_buffer
      - .actual_access:  read_only
        .address_space:  global
        .offset:         32
        .size:           8
        .value_kind:     global_buffer
      - .actual_access:  read_only
        .address_space:  global
        .offset:         40
        .size:           8
        .value_kind:     global_buffer
      - .actual_access:  write_only
        .address_space:  global
        .offset:         48
        .size:           8
        .value_kind:     global_buffer
      - .actual_access:  write_only
        .address_space:  global
        .offset:         56
        .size:           8
        .value_kind:     global_buffer
    .group_segment_fixed_size: 81664
    .kernarg_segment_align: 8
    .kernarg_segment_size: 64
    .language:       OpenCL C
    .language_version:
      - 2
      - 0
    .max_flat_workgroup_size: 256
    .name:           _Z10gae_kernelPKfPKiS2_S0_S0_S0_PfS3_
    .private_segment_fixed_size: 0
    .sgpr_count:     22
    .sgpr_spill_count: 0
    .symbol:         _Z10gae_kernelPKfPKiS2_S0_S0_S0_PfS3_.kd
    .uniform_work_group_size: 1
    .uses_dynamic_stack: false
    .vgpr_count:     74
    .vgpr_spill_count: 0
    .wavefront_size: 64
